# scan_s1 loop by hand: dwordx4 row loads + permlane transposes (32 loads per item instead of 128)
# baseline (speedup 1.0000x reference)
; __device__ __forceinline__ float bf_lo(unsigned w) { return __uint_as_float(w << 16); }
; __device__ __forceinline__ float bf_hi(unsigned w) { return __uint_as_float(w & 0xffff0000u); }
; __device__ __forceinline__ void scan_s1(CTXA) {
;     ...
;     for (int it = F.gw; it < 2 * NB * 64 * 8; it += F.NGW) {
;         const int cg = it & 7, chunk = (it >> 3) & 63, b = (it >> 9) & 3, d = it >> 11;
;         const int ch = cg * 128 + 2 * F.lane;
;         const size_t e0 = (size_t)d * T * D + ((size_t)b * S + chunk * 64) * D + ch;
;         const unsigned* la = (const unsigned*)(LA + e0); const unsigned* bb = (const unsigned*)(BB + e0);
;         float A0 = 0.f, A1 = 0.f, B0 = 0.f, B1 = 0.f;
; #pragma unroll
;         for (int g = 0; g < 4; ++g) { unsigned wl[16], wb[16];
; #pragma unroll
;             for (int q = 0; q < 16; ++q) { const int tt = g * 16 + q, t = d ? 63 - tt : tt; wl[q] = la[(size_t)t * (D / 2)]; wb[q] = bb[(size_t)t * (D / 2)]; }
; #pragma unroll
;             for (int q = 0; q < 16; ++q) { const float l0 = bf_lo(wl[q]), l1 = bf_hi(wl[q]);
;                 A0 += l0; A1 += l1; B0 = __expf(l0) * B0 + bf_lo(wb[q]); B1 = __expf(l1) * B1 + bf_hi(wb[q]); } }
.LBB0_192:
	s_ashr_i32 s6, s0, 6
	s_lshl_b32 s0, s2, 3
	s_add_i32 s0, s0, s6
	s_cmpk_gt_i32 s0, 0xfff
	s_mov_b32 s27, 0x1e800
	s_movk_i32 s28, 0x1800
	s_mov_b32 s29, 0x1d800
	s_movk_i32 s35, 0x2800
	s_mov_b32 s38, 0x1c800
	s_movk_i32 s42, 0x3800
	s_mov_b32 s43, 0x1b800
	s_movk_i32 s44, 0x4800
	s_mov_b32 s45, 0x1a800
	s_movk_i32 s46, 0x5800
	s_mov_b32 s47, 0x19800
	s_movk_i32 s48, 0x6800
	s_mov_b32 s49, 0x18800
	s_movk_i32 s50, 0x7800
	s_mov_b32 s51, 0x17800
	s_cbranch_scc1 .LBB0_195
	v_readlane_b32 s12, v254, 51
	s_lshl_b32 s1, s34, 3
	s_ashr_i32 s8, s7, 31
	v_readlane_b32 s14, v254, 53
	v_readlane_b32 s15, v254, 54
	s_add_u32 s7, s14, s7
	s_addc_u32 s8, s15, s8
	s_add_u32 s10, s7, 0x2c400000
	s_addc_u32 s11, s8, 0
	s_add_u32 s30, s7, 0x30400000
	s_addc_u32 s31, s8, 0
	s_add_u32 s36, s7, 0x36400000
	s_addc_u32 s37, s8, 0
	s_add_u32 s40, s7, 0x36600000
	s_addc_u32 s41, s8, 0
	v_lshlrev_b32_e32 v1, 1, v1
	s_lshl_b32 s2, s2, 10
	s_lshl_b32 s6, s6, 7
	v_and_b32_e32 v1, 15, v238
	v_bfe_u32 v2, v238, 4, 2
	v_lshlrev_b32_e32 v1, 3, v1
	v_lshl_or_b32 v1, v2, 1, v1
	s_add_i32 s6, s2, s6
	s_lshl_b32 s7, s34, 10
	v_readlane_b32 s13, v254, 52
.LBB0_194:
	s_bfe_u32 s8, s0, 0x60003
	s_bfe_u32 s9, s0, 0x20009
	s_ashr_i32 s16, s0, 11
	s_and_b32 s2, s6, 0x380
	v_or_b32_e32 v14, s2, v1
	s_lshl_b32 s2, s9, 22
	s_lshl_b32 s14, s8, 16
	s_or_b32 s2, s2, s14
	s_lshl_b32 s14, s16, 24
	s_or_b32 s2, s2, s14
	s_mul_i32 s14, s16, 63
	v_bfe_u32 v9, v1, 1, 2
	v_and_b32_e32 v8, 0xfffffff9, v14
	v_xor_b32_e32 v9, s14, v9
	v_or_b32_e32 v8, s2, v8
	v_lshlrev_b32_e32 v8, 1, v8
	v_lshl_add_u32 v8, v9, 11, v8
	s_movk_i32 s17, 0x2000
	s_cmp_lg_u32 s16, 0
	s_cselect_b32 s17, 0xffffe000, s17
	v_mov_b32_e32 v2, 0
	v_mov_b32_e32 v3, 0
	v_mov_b32_e32 v4, 0
	v_mov_b32_e32 v5, 0
	global_load_dwordx4 v[18:21], v8, s[10:11]
	global_load_dwordx4 v[22:25], v8, s[30:31]
	v_add_u32_e32 v8, s17, v8
	global_load_dwordx4 v[26:29], v8, s[10:11]
	global_load_dwordx4 v[30:33], v8, s[30:31]
	v_add_u32_e32 v8, s17, v8
	global_load_dwordx4 v[34:37], v8, s[10:11]
	global_load_dwordx4 v[38:41], v8, s[30:31]
	v_add_u32_e32 v8, s17, v8
	global_load_dwordx4 v[42:45], v8, s[10:11]
	global_load_dwordx4 v[46:49], v8, s[30:31]
	v_add_u32_e32 v8, s17, v8
	global_load_dwordx4 v[50:53], v8, s[10:11]
	global_load_dwordx4 v[54:57], v8, s[30:31]
	v_add_u32_e32 v8, s17, v8
	global_load_dwordx4 v[58:61], v8, s[10:11]
	global_load_dwordx4 v[62:65], v8, s[30:31]
	v_add_u32_e32 v8, s17, v8
	global_load_dwordx4 v[68:71], v8, s[10:11]
	global_load_dwordx4 v[72:75], v8, s[30:31]
	v_add_u32_e32 v8, s17, v8
	global_load_dwordx4 v[76:79], v8, s[10:11]
	global_load_dwordx4 v[80:83], v8, s[30:31]
	v_add_u32_e32 v8, s17, v8
	s_waitcnt vmcnt(14)
	v_permlane16_swap_b32_e32 v18, v19
	v_permlane16_swap_b32_e32 v20, v21
	v_permlane16_swap_b32_e32 v22, v23
	v_permlane16_swap_b32_e32 v24, v25
	v_permlane32_swap_b32_e32 v18, v20
	v_permlane32_swap_b32_e32 v19, v21
	v_permlane32_swap_b32_e32 v22, v24
	v_permlane32_swap_b32_e32 v23, v25
	v_and_b32_e32 v10, 0xffff0000, v18
	v_lshlrev_b32_e32 v18, 16, v18
	v_and_b32_e32 v11, 0xffff0000, v19
	v_lshlrev_b32_e32 v19, 16, v19
	v_and_b32_e32 v12, 0xffff0000, v20
	v_lshlrev_b32_e32 v20, 16, v20
	v_and_b32_e32 v13, 0xffff0000, v21
	v_lshlrev_b32_e32 v21, 16, v21
	v_add_f32_e32 v2, v2, v18
	v_add_f32_e32 v3, v3, v10
	v_add_f32_e32 v2, v2, v19
	v_add_f32_e32 v3, v3, v11
	v_add_f32_e32 v2, v2, v20
	v_add_f32_e32 v3, v3, v12
	v_add_f32_e32 v2, v2, v21
	v_add_f32_e32 v3, v3, v13
	v_mul_f32_e32 v18, 0x3fb8aa3b, v18
	v_mul_f32_e32 v10, 0x3fb8aa3b, v10
	v_mul_f32_e32 v19, 0x3fb8aa3b, v19
	v_mul_f32_e32 v11, 0x3fb8aa3b, v11
	v_mul_f32_e32 v20, 0x3fb8aa3b, v20
	v_mul_f32_e32 v12, 0x3fb8aa3b, v12
	v_mul_f32_e32 v21, 0x3fb8aa3b, v21
	v_mul_f32_e32 v13, 0x3fb8aa3b, v13
	v_exp_f32_e32 v18, v18
	v_exp_f32_e32 v10, v10
	v_exp_f32_e32 v19, v19
	v_exp_f32_e32 v11, v11
	v_exp_f32_e32 v20, v20
	v_exp_f32_e32 v12, v12
	v_exp_f32_e32 v21, v21
	v_exp_f32_e32 v13, v13
	v_lshlrev_b32_e32 v6, 16, v22
	v_and_b32_e32 v7, 0xffff0000, v22
	v_fmac_f32_e32 v6, v4, v18
	v_fmac_f32_e32 v7, v5, v10
	v_lshlrev_b32_e32 v4, 16, v23
	v_and_b32_e32 v5, 0xffff0000, v23
	v_fmac_f32_e32 v4, v6, v19
	v_fmac_f32_e32 v5, v7, v11
	v_lshlrev_b32_e32 v6, 16, v24
	v_and_b32_e32 v7, 0xffff0000, v24
	v_fmac_f32_e32 v6, v4, v20
	v_fmac_f32_e32 v7, v5, v12
	v_lshlrev_b32_e32 v4, 16, v25
	v_and_b32_e32 v5, 0xffff0000, v25
	v_fmac_f32_e32 v4, v6, v21
	v_fmac_f32_e32 v5, v7, v13
	global_load_dwordx4 v[18:21], v8, s[10:11]
	global_load_dwordx4 v[22:25], v8, s[30:31]
	v_add_u32_e32 v8, s17, v8
	s_waitcnt vmcnt(14)
	v_permlane16_swap_b32_e32 v26, v27
	v_permlane16_swap_b32_e32 v28, v29
	v_permlane16_swap_b32_e32 v30, v31
	v_permlane16_swap_b32_e32 v32, v33
	v_permlane32_swap_b32_e32 v26, v28
	v_permlane32_swap_b32_e32 v27, v29
	v_permlane32_swap_b32_e32 v30, v32
	v_permlane32_swap_b32_e32 v31, v33
	v_and_b32_e32 v10, 0xffff0000, v26
	v_lshlrev_b32_e32 v26, 16, v26
	v_and_b32_e32 v11, 0xffff0000, v27
	v_lshlrev_b32_e32 v27, 16, v27
	v_and_b32_e32 v12, 0xffff0000, v28
	v_lshlrev_b32_e32 v28, 16, v28
	v_and_b32_e32 v13, 0xffff0000, v29
	v_lshlrev_b32_e32 v29, 16, v29
	v_add_f32_e32 v2, v2, v26
	v_add_f32_e32 v3, v3, v10
	v_add_f32_e32 v2, v2, v27
	v_add_f32_e32 v3, v3, v11
	v_add_f32_e32 v2, v2, v28
	v_add_f32_e32 v3, v3, v12
	v_add_f32_e32 v2, v2, v29
	v_add_f32_e32 v3, v3, v13
	v_mul_f32_e32 v26, 0x3fb8aa3b, v26
	v_mul_f32_e32 v10, 0x3fb8aa3b, v10
	v_mul_f32_e32 v27, 0x3fb8aa3b, v27
	v_mul_f32_e32 v11, 0x3fb8aa3b, v11
	v_mul_f32_e32 v28, 0x3fb8aa3b, v28
	v_mul_f32_e32 v12, 0x3fb8aa3b, v12
	v_mul_f32_e32 v29, 0x3fb8aa3b, v29
	v_mul_f32_e32 v13, 0x3fb8aa3b, v13
	v_exp_f32_e32 v26, v26
	v_exp_f32_e32 v10, v10
	v_exp_f32_e32 v27, v27
	v_exp_f32_e32 v11, v11
	v_exp_f32_e32 v28, v28
	v_exp_f32_e32 v12, v12
	v_exp_f32_e32 v29, v29
	v_exp_f32_e32 v13, v13
	v_lshlrev_b32_e32 v6, 16, v30
	v_and_b32_e32 v7, 0xffff0000, v30
	v_fmac_f32_e32 v6, v4, v26
	v_fmac_f32_e32 v7, v5, v10
	v_lshlrev_b32_e32 v4, 16, v31
	v_and_b32_e32 v5, 0xffff0000, v31
	v_fmac_f32_e32 v4, v6, v27
	v_fmac_f32_e32 v5, v7, v11
	v_lshlrev_b32_e32 v6, 16, v32
	v_and_b32_e32 v7, 0xffff0000, v32
	v_fmac_f32_e32 v6, v4, v28
	v_fmac_f32_e32 v7, v5, v12
	v_lshlrev_b32_e32 v4, 16, v33
	v_and_b32_e32 v5, 0xffff0000, v33
	v_fmac_f32_e32 v4, v6, v29
	v_fmac_f32_e32 v5, v7, v13
	global_load_dwordx4 v[26:29], v8, s[10:11]
	global_load_dwordx4 v[30:33], v8, s[30:31]
	v_add_u32_e32 v8, s17, v8
	s_waitcnt vmcnt(14)
; __device__ __forceinline__ float bf_lo(unsigned w) { return __uint_as_float(w << 16); }
; __device__ __forceinline__ float bf_hi(unsigned w) { return __uint_as_float(w & 0xffff0000u); }
; __device__ __forceinline__ void scan_s1(CTXA) {
;     ...
;         for (int g = 0; g < 4; ++g) { unsigned wl[16], wb[16];
; #pragma unroll
;             for (int q = 0; q < 16; ++q) { const int tt = g * 16 + q, t = d ? 63 - tt : tt; wl[q] = la[(size_t)t * (D / 2)]; wb[q] = bb[(size_t)t * (D / 2)]; }
; #pragma unroll
;             for (int q = 0; q < 16; ++q) { const float l0 = bf_lo(wl[q]), l1 = bf_hi(wl[q]);
;                 A0 += l0; A1 += l1; B0 = __expf(l0) * B0 + bf_lo(wb[q]); B1 = __expf(l1) * B1 + bf_hi(wb[q]); } }
	v_permlane16_swap_b32_e32 v34, v35
	v_permlane16_swap_b32_e32 v36, v37
	v_permlane16_swap_b32_e32 v38, v39
	v_permlane16_swap_b32_e32 v40, v41
	v_permlane32_swap_b32_e32 v34, v36
	v_permlane32_swap_b32_e32 v35, v37
	v_permlane32_swap_b32_e32 v38, v40
	v_permlane32_swap_b32_e32 v39, v41
	v_and_b32_e32 v10, 0xffff0000, v34
	v_lshlrev_b32_e32 v34, 16, v34
	v_and_b32_e32 v11, 0xffff0000, v35
	v_lshlrev_b32_e32 v35, 16, v35
	v_and_b32_e32 v12, 0xffff0000, v36
	v_lshlrev_b32_e32 v36, 16, v36
	v_and_b32_e32 v13, 0xffff0000, v37
	v_lshlrev_b32_e32 v37, 16, v37
	v_add_f32_e32 v2, v2, v34
	v_add_f32_e32 v3, v3, v10
	v_add_f32_e32 v2, v2, v35
	v_add_f32_e32 v3, v3, v11
	v_add_f32_e32 v2, v2, v36
	v_add_f32_e32 v3, v3, v12
	v_add_f32_e32 v2, v2, v37
	v_add_f32_e32 v3, v3, v13
	v_mul_f32_e32 v34, 0x3fb8aa3b, v34
	v_mul_f32_e32 v10, 0x3fb8aa3b, v10
	v_mul_f32_e32 v35, 0x3fb8aa3b, v35
	v_mul_f32_e32 v11, 0x3fb8aa3b, v11
	v_mul_f32_e32 v36, 0x3fb8aa3b, v36
	v_mul_f32_e32 v12, 0x3fb8aa3b, v12
	v_mul_f32_e32 v37, 0x3fb8aa3b, v37
	v_mul_f32_e32 v13, 0x3fb8aa3b, v13
	v_exp_f32_e32 v34, v34
	v_exp_f32_e32 v10, v10
	v_exp_f32_e32 v35, v35
	v_exp_f32_e32 v11, v11
	v_exp_f32_e32 v36, v36
	v_exp_f32_e32 v12, v12
	v_exp_f32_e32 v37, v37
	v_exp_f32_e32 v13, v13
	v_lshlrev_b32_e32 v6, 16, v38
	v_and_b32_e32 v7, 0xffff0000, v38
	v_fmac_f32_e32 v6, v4, v34
	v_fmac_f32_e32 v7, v5, v10
	v_lshlrev_b32_e32 v4, 16, v39
	v_and_b32_e32 v5, 0xffff0000, v39
	v_fmac_f32_e32 v4, v6, v35
	v_fmac_f32_e32 v5, v7, v11
	v_lshlrev_b32_e32 v6, 16, v40
	v_and_b32_e32 v7, 0xffff0000, v40
	v_fmac_f32_e32 v6, v4, v36
	v_fmac_f32_e32 v7, v5, v12
	v_lshlrev_b32_e32 v4, 16, v41
	v_and_b32_e32 v5, 0xffff0000, v41
	v_fmac_f32_e32 v4, v6, v37
	v_fmac_f32_e32 v5, v7, v13
	global_load_dwordx4 v[34:37], v8, s[10:11]
	global_load_dwordx4 v[38:41], v8, s[30:31]
	v_add_u32_e32 v8, s17, v8
	s_waitcnt vmcnt(14)
	v_permlane16_swap_b32_e32 v42, v43
	v_permlane16_swap_b32_e32 v44, v45
	v_permlane16_swap_b32_e32 v46, v47
	v_permlane16_swap_b32_e32 v48, v49
	v_permlane32_swap_b32_e32 v42, v44
	v_permlane32_swap_b32_e32 v43, v45
	v_permlane32_swap_b32_e32 v46, v48
	v_permlane32_swap_b32_e32 v47, v49
	v_and_b32_e32 v10, 0xffff0000, v42
	v_lshlrev_b32_e32 v42, 16, v42
	v_and_b32_e32 v11, 0xffff0000, v43
	v_lshlrev_b32_e32 v43, 16, v43
	v_and_b32_e32 v12, 0xffff0000, v44
	v_lshlrev_b32_e32 v44, 16, v44
	v_and_b32_e32 v13, 0xffff0000, v45
	v_lshlrev_b32_e32 v45, 16, v45
	v_add_f32_e32 v2, v2, v42
	v_add_f32_e32 v3, v3, v10
	v_add_f32_e32 v2, v2, v43
	v_add_f32_e32 v3, v3, v11
	v_add_f32_e32 v2, v2, v44
	v_add_f32_e32 v3, v3, v12
	v_add_f32_e32 v2, v2, v45
	v_add_f32_e32 v3, v3, v13
	v_mul_f32_e32 v42, 0x3fb8aa3b, v42
	v_mul_f32_e32 v10, 0x3fb8aa3b, v10
	v_mul_f32_e32 v43, 0x3fb8aa3b, v43
	v_mul_f32_e32 v11, 0x3fb8aa3b, v11
	v_mul_f32_e32 v44, 0x3fb8aa3b, v44
	v_mul_f32_e32 v12, 0x3fb8aa3b, v12
	v_mul_f32_e32 v45, 0x3fb8aa3b, v45
	v_mul_f32_e32 v13, 0x3fb8aa3b, v13
	v_exp_f32_e32 v42, v42
	v_exp_f32_e32 v10, v10
	v_exp_f32_e32 v43, v43
	v_exp_f32_e32 v11, v11
	v_exp_f32_e32 v44, v44
	v_exp_f32_e32 v12, v12
	v_exp_f32_e32 v45, v45
	v_exp_f32_e32 v13, v13
	v_lshlrev_b32_e32 v6, 16, v46
	v_and_b32_e32 v7, 0xffff0000, v46
	v_fmac_f32_e32 v6, v4, v42
	v_fmac_f32_e32 v7, v5, v10
	v_lshlrev_b32_e32 v4, 16, v47
	v_and_b32_e32 v5, 0xffff0000, v47
	v_fmac_f32_e32 v4, v6, v43
	v_fmac_f32_e32 v5, v7, v11
	v_lshlrev_b32_e32 v6, 16, v48
	v_and_b32_e32 v7, 0xffff0000, v48
	v_fmac_f32_e32 v6, v4, v44
	v_fmac_f32_e32 v7, v5, v12
	v_lshlrev_b32_e32 v4, 16, v49
	v_and_b32_e32 v5, 0xffff0000, v49
	v_fmac_f32_e32 v4, v6, v45
	v_fmac_f32_e32 v5, v7, v13
	global_load_dwordx4 v[42:45], v8, s[10:11]
	global_load_dwordx4 v[46:49], v8, s[30:31]
	v_add_u32_e32 v8, s17, v8
	s_waitcnt vmcnt(14)
	v_permlane16_swap_b32_e32 v50, v51
	v_permlane16_swap_b32_e32 v52, v53
	v_permlane16_swap_b32_e32 v54, v55
	v_permlane16_swap_b32_e32 v56, v57
	v_permlane32_swap_b32_e32 v50, v52
	v_permlane32_swap_b32_e32 v51, v53
	v_permlane32_swap_b32_e32 v54, v56
	v_permlane32_swap_b32_e32 v55, v57
	v_and_b32_e32 v10, 0xffff0000, v50
	v_lshlrev_b32_e32 v50, 16, v50
	v_and_b32_e32 v11, 0xffff0000, v51
	v_lshlrev_b32_e32 v51, 16, v51
	v_and_b32_e32 v12, 0xffff0000, v52
	v_lshlrev_b32_e32 v52, 16, v52
	v_and_b32_e32 v13, 0xffff0000, v53
	v_lshlrev_b32_e32 v53, 16, v53
	v_add_f32_e32 v2, v2, v50
	v_add_f32_e32 v3, v3, v10
	v_add_f32_e32 v2, v2, v51
	v_add_f32_e32 v3, v3, v11
	v_add_f32_e32 v2, v2, v52
	v_add_f32_e32 v3, v3, v12
	v_add_f32_e32 v2, v2, v53
	v_add_f32_e32 v3, v3, v13
	v_mul_f32_e32 v50, 0x3fb8aa3b, v50
	v_mul_f32_e32 v10, 0x3fb8aa3b, v10
	v_mul_f32_e32 v51, 0x3fb8aa3b, v51
	v_mul_f32_e32 v11, 0x3fb8aa3b, v11
	v_mul_f32_e32 v52, 0x3fb8aa3b, v52
	v_mul_f32_e32 v12, 0x3fb8aa3b, v12
	v_mul_f32_e32 v53, 0x3fb8aa3b, v53
	v_mul_f32_e32 v13, 0x3fb8aa3b, v13
	v_exp_f32_e32 v50, v50
	v_exp_f32_e32 v10, v10
	v_exp_f32_e32 v51, v51
	v_exp_f32_e32 v11, v11
	v_exp_f32_e32 v52, v52
	v_exp_f32_e32 v12, v12
	v_exp_f32_e32 v53, v53
	v_exp_f32_e32 v13, v13
	v_lshlrev_b32_e32 v6, 16, v54
	v_and_b32_e32 v7, 0xffff0000, v54
	v_fmac_f32_e32 v6, v4, v50
	v_fmac_f32_e32 v7, v5, v10
	v_lshlrev_b32_e32 v4, 16, v55
	v_and_b32_e32 v5, 0xffff0000, v55
	v_fmac_f32_e32 v4, v6, v51
	v_fmac_f32_e32 v5, v7, v11
	v_lshlrev_b32_e32 v6, 16, v56
	v_and_b32_e32 v7, 0xffff0000, v56
	v_fmac_f32_e32 v6, v4, v52
	v_fmac_f32_e32 v7, v5, v12
	v_lshlrev_b32_e32 v4, 16, v57
	v_and_b32_e32 v5, 0xffff0000, v57
	v_fmac_f32_e32 v4, v6, v53
	v_fmac_f32_e32 v5, v7, v13
	global_load_dwordx4 v[50:53], v8, s[10:11]
	global_load_dwordx4 v[54:57], v8, s[30:31]
	v_add_u32_e32 v8, s17, v8
	s_waitcnt vmcnt(14)
; __device__ __forceinline__ float bf_lo(unsigned w) { return __uint_as_float(w << 16); }
; __device__ __forceinline__ float bf_hi(unsigned w) { return __uint_as_float(w & 0xffff0000u); }
; __device__ __forceinline__ void scan_s1(CTXA) {
;     ...
;         for (int g = 0; g < 4; ++g) { unsigned wl[16], wb[16];
; #pragma unroll
;             for (int q = 0; q < 16; ++q) { const int tt = g * 16 + q, t = d ? 63 - tt : tt; wl[q] = la[(size_t)t * (D / 2)]; wb[q] = bb[(size_t)t * (D / 2)]; }
; #pragma unroll
;             for (int q = 0; q < 16; ++q) { const float l0 = bf_lo(wl[q]), l1 = bf_hi(wl[q]);
;                 A0 += l0; A1 += l1; B0 = __expf(l0) * B0 + bf_lo(wb[q]); B1 = __expf(l1) * B1 + bf_hi(wb[q]); } }
	v_permlane16_swap_b32_e32 v58, v59
	v_permlane16_swap_b32_e32 v60, v61
	v_permlane16_swap_b32_e32 v62, v63
	v_permlane16_swap_b32_e32 v64, v65
	v_permlane32_swap_b32_e32 v58, v60
	v_permlane32_swap_b32_e32 v59, v61
	v_permlane32_swap_b32_e32 v62, v64
	v_permlane32_swap_b32_e32 v63, v65
	v_and_b32_e32 v10, 0xffff0000, v58
	v_lshlrev_b32_e32 v58, 16, v58
	v_and_b32_e32 v11, 0xffff0000, v59
	v_lshlrev_b32_e32 v59, 16, v59
	v_and_b32_e32 v12, 0xffff0000, v60
	v_lshlrev_b32_e32 v60, 16, v60
	v_and_b32_e32 v13, 0xffff0000, v61
	v_lshlrev_b32_e32 v61, 16, v61
	v_add_f32_e32 v2, v2, v58
	v_add_f32_e32 v3, v3, v10
	v_add_f32_e32 v2, v2, v59
	v_add_f32_e32 v3, v3, v11
	v_add_f32_e32 v2, v2, v60
	v_add_f32_e32 v3, v3, v12
	v_add_f32_e32 v2, v2, v61
	v_add_f32_e32 v3, v3, v13
	v_mul_f32_e32 v58, 0x3fb8aa3b, v58
	v_mul_f32_e32 v10, 0x3fb8aa3b, v10
	v_mul_f32_e32 v59, 0x3fb8aa3b, v59
	v_mul_f32_e32 v11, 0x3fb8aa3b, v11
	v_mul_f32_e32 v60, 0x3fb8aa3b, v60
	v_mul_f32_e32 v12, 0x3fb8aa3b, v12
	v_mul_f32_e32 v61, 0x3fb8aa3b, v61
	v_mul_f32_e32 v13, 0x3fb8aa3b, v13
	v_exp_f32_e32 v58, v58
	v_exp_f32_e32 v10, v10
	v_exp_f32_e32 v59, v59
	v_exp_f32_e32 v11, v11
	v_exp_f32_e32 v60, v60
	v_exp_f32_e32 v12, v12
	v_exp_f32_e32 v61, v61
	v_exp_f32_e32 v13, v13
	v_lshlrev_b32_e32 v6, 16, v62
	v_and_b32_e32 v7, 0xffff0000, v62
	v_fmac_f32_e32 v6, v4, v58
	v_fmac_f32_e32 v7, v5, v10
	v_lshlrev_b32_e32 v4, 16, v63
	v_and_b32_e32 v5, 0xffff0000, v63
	v_fmac_f32_e32 v4, v6, v59
	v_fmac_f32_e32 v5, v7, v11
	v_lshlrev_b32_e32 v6, 16, v64
	v_and_b32_e32 v7, 0xffff0000, v64
	v_fmac_f32_e32 v6, v4, v60
	v_fmac_f32_e32 v7, v5, v12
	v_lshlrev_b32_e32 v4, 16, v65
	v_and_b32_e32 v5, 0xffff0000, v65
	v_fmac_f32_e32 v4, v6, v61
	v_fmac_f32_e32 v5, v7, v13
	global_load_dwordx4 v[58:61], v8, s[10:11]
	global_load_dwordx4 v[62:65], v8, s[30:31]
	v_add_u32_e32 v8, s17, v8
	s_waitcnt vmcnt(14)
	v_permlane16_swap_b32_e32 v68, v69
	v_permlane16_swap_b32_e32 v70, v71
	v_permlane16_swap_b32_e32 v72, v73
	v_permlane16_swap_b32_e32 v74, v75
	v_permlane32_swap_b32_e32 v68, v70
	v_permlane32_swap_b32_e32 v69, v71
	v_permlane32_swap_b32_e32 v72, v74
	v_permlane32_swap_b32_e32 v73, v75
	v_and_b32_e32 v10, 0xffff0000, v68
	v_lshlrev_b32_e32 v68, 16, v68
	v_and_b32_e32 v11, 0xffff0000, v69
	v_lshlrev_b32_e32 v69, 16, v69
	v_and_b32_e32 v12, 0xffff0000, v70
	v_lshlrev_b32_e32 v70, 16, v70
	v_and_b32_e32 v13, 0xffff0000, v71
	v_lshlrev_b32_e32 v71, 16, v71
	v_add_f32_e32 v2, v2, v68
	v_add_f32_e32 v3, v3, v10
	v_add_f32_e32 v2, v2, v69
	v_add_f32_e32 v3, v3, v11
	v_add_f32_e32 v2, v2, v70
	v_add_f32_e32 v3, v3, v12
	v_add_f32_e32 v2, v2, v71
	v_add_f32_e32 v3, v3, v13
	v_mul_f32_e32 v68, 0x3fb8aa3b, v68
	v_mul_f32_e32 v10, 0x3fb8aa3b, v10
	v_mul_f32_e32 v69, 0x3fb8aa3b, v69
	v_mul_f32_e32 v11, 0x3fb8aa3b, v11
	v_mul_f32_e32 v70, 0x3fb8aa3b, v70
	v_mul_f32_e32 v12, 0x3fb8aa3b, v12
	v_mul_f32_e32 v71, 0x3fb8aa3b, v71
	v_mul_f32_e32 v13, 0x3fb8aa3b, v13
	v_exp_f32_e32 v68, v68
	v_exp_f32_e32 v10, v10
	v_exp_f32_e32 v69, v69
	v_exp_f32_e32 v11, v11
	v_exp_f32_e32 v70, v70
	v_exp_f32_e32 v12, v12
	v_exp_f32_e32 v71, v71
	v_exp_f32_e32 v13, v13
	v_lshlrev_b32_e32 v6, 16, v72
	v_and_b32_e32 v7, 0xffff0000, v72
	v_fmac_f32_e32 v6, v4, v68
	v_fmac_f32_e32 v7, v5, v10
	v_lshlrev_b32_e32 v4, 16, v73
	v_and_b32_e32 v5, 0xffff0000, v73
	v_fmac_f32_e32 v4, v6, v69
	v_fmac_f32_e32 v5, v7, v11
	v_lshlrev_b32_e32 v6, 16, v74
	v_and_b32_e32 v7, 0xffff0000, v74
	v_fmac_f32_e32 v6, v4, v70
	v_fmac_f32_e32 v7, v5, v12
	v_lshlrev_b32_e32 v4, 16, v75
	v_and_b32_e32 v5, 0xffff0000, v75
	v_fmac_f32_e32 v4, v6, v71
	v_fmac_f32_e32 v5, v7, v13
	global_load_dwordx4 v[68:71], v8, s[10:11]
	global_load_dwordx4 v[72:75], v8, s[30:31]
	v_add_u32_e32 v8, s17, v8
	s_waitcnt vmcnt(14)
	v_permlane16_swap_b32_e32 v76, v77
	v_permlane16_swap_b32_e32 v78, v79
	v_permlane16_swap_b32_e32 v80, v81
	v_permlane16_swap_b32_e32 v82, v83
	v_permlane32_swap_b32_e32 v76, v78
	v_permlane32_swap_b32_e32 v77, v79
	v_permlane32_swap_b32_e32 v80, v82
	v_permlane32_swap_b32_e32 v81, v83
	v_and_b32_e32 v10, 0xffff0000, v76
	v_lshlrev_b32_e32 v76, 16, v76
	v_and_b32_e32 v11, 0xffff0000, v77
	v_lshlrev_b32_e32 v77, 16, v77
	v_and_b32_e32 v12, 0xffff0000, v78
	v_lshlrev_b32_e32 v78, 16, v78
	v_and_b32_e32 v13, 0xffff0000, v79
	v_lshlrev_b32_e32 v79, 16, v79
	v_add_f32_e32 v2, v2, v76
	v_add_f32_e32 v3, v3, v10
	v_add_f32_e32 v2, v2, v77
	v_add_f32_e32 v3, v3, v11
	v_add_f32_e32 v2, v2, v78
	v_add_f32_e32 v3, v3, v12
	v_add_f32_e32 v2, v2, v79
	v_add_f32_e32 v3, v3, v13
	v_mul_f32_e32 v76, 0x3fb8aa3b, v76
	v_mul_f32_e32 v10, 0x3fb8aa3b, v10
	v_mul_f32_e32 v77, 0x3fb8aa3b, v77
	v_mul_f32_e32 v11, 0x3fb8aa3b, v11
	v_mul_f32_e32 v78, 0x3fb8aa3b, v78
	v_mul_f32_e32 v12, 0x3fb8aa3b, v12
	v_mul_f32_e32 v79, 0x3fb8aa3b, v79
	v_mul_f32_e32 v13, 0x3fb8aa3b, v13
	v_exp_f32_e32 v76, v76
	v_exp_f32_e32 v10, v10
	v_exp_f32_e32 v77, v77
	v_exp_f32_e32 v11, v11
	v_exp_f32_e32 v78, v78
	v_exp_f32_e32 v12, v12
	v_exp_f32_e32 v79, v79
	v_exp_f32_e32 v13, v13
	v_lshlrev_b32_e32 v6, 16, v80
	v_and_b32_e32 v7, 0xffff0000, v80
	v_fmac_f32_e32 v6, v4, v76
	v_fmac_f32_e32 v7, v5, v10
	v_lshlrev_b32_e32 v4, 16, v81
	v_and_b32_e32 v5, 0xffff0000, v81
	v_fmac_f32_e32 v4, v6, v77
	v_fmac_f32_e32 v5, v7, v11
	v_lshlrev_b32_e32 v6, 16, v82
	v_and_b32_e32 v7, 0xffff0000, v82
	v_fmac_f32_e32 v6, v4, v78
	v_fmac_f32_e32 v7, v5, v12
	v_lshlrev_b32_e32 v4, 16, v83
	v_and_b32_e32 v5, 0xffff0000, v83
	v_fmac_f32_e32 v4, v6, v79
	v_fmac_f32_e32 v5, v7, v13
	global_load_dwordx4 v[76:79], v8, s[10:11]
	global_load_dwordx4 v[80:83], v8, s[30:31]
	s_waitcnt vmcnt(14)
; __device__ __forceinline__ float bf_lo(unsigned w) { return __uint_as_float(w << 16); }
; __device__ __forceinline__ float bf_hi(unsigned w) { return __uint_as_float(w & 0xffff0000u); }
; __device__ __forceinline__ void scan_s1(CTXA) {
;     ...
;     for (int it = F.gw; it < 2 * NB * 64 * 8; it += F.NGW) {
;         const int cg = it & 7, chunk = (it >> 3) & 63, b = (it >> 9) & 3, d = it >> 11;
;         const int ch = cg * 128 + 2 * F.lane;
;         const size_t e0 = (size_t)d * T * D + ((size_t)b * S + chunk * 64) * D + ch;
;         const unsigned* la = (const unsigned*)(LA + e0); const unsigned* bb = (const unsigned*)(BB + e0);
;         float A0 = 0.f, A1 = 0.f, B0 = 0.f, B1 = 0.f;
; #pragma unroll
;         for (int g = 0; g < 4; ++g) { unsigned wl[16], wb[16];
; #pragma unroll
;             for (int q = 0; q < 16; ++q) { const int tt = g * 16 + q, t = d ? 63 - tt : tt; wl[q] = la[(size_t)t * (D / 2)]; wb[q] = bb[(size_t)t * (D / 2)]; }
; #pragma unroll
;             for (int q = 0; q < 16; ++q) { const float l0 = bf_lo(wl[q]), l1 = bf_hi(wl[q]);
;                 A0 += l0; A1 += l1; B0 = __expf(l0) * B0 + bf_lo(wb[q]); B1 = __expf(l1) * B1 + bf_hi(wb[q]); } }
	v_permlane16_swap_b32_e32 v18, v19
	v_permlane16_swap_b32_e32 v20, v21
	v_permlane16_swap_b32_e32 v22, v23
	v_permlane16_swap_b32_e32 v24, v25
	v_permlane32_swap_b32_e32 v18, v20
	v_permlane32_swap_b32_e32 v19, v21
	v_permlane32_swap_b32_e32 v22, v24
	v_permlane32_swap_b32_e32 v23, v25
	v_and_b32_e32 v10, 0xffff0000, v18
	v_lshlrev_b32_e32 v18, 16, v18
	v_and_b32_e32 v11, 0xffff0000, v19
	v_lshlrev_b32_e32 v19, 16, v19
	v_and_b32_e32 v12, 0xffff0000, v20
	v_lshlrev_b32_e32 v20, 16, v20
	v_and_b32_e32 v13, 0xffff0000, v21
	v_lshlrev_b32_e32 v21, 16, v21
	v_add_f32_e32 v2, v2, v18
	v_add_f32_e32 v3, v3, v10
	v_add_f32_e32 v2, v2, v19
	v_add_f32_e32 v3, v3, v11
	v_add_f32_e32 v2, v2, v20
	v_add_f32_e32 v3, v3, v12
	v_add_f32_e32 v2, v2, v21
	v_add_f32_e32 v3, v3, v13
	v_mul_f32_e32 v18, 0x3fb8aa3b, v18
	v_mul_f32_e32 v10, 0x3fb8aa3b, v10
	v_mul_f32_e32 v19, 0x3fb8aa3b, v19
	v_mul_f32_e32 v11, 0x3fb8aa3b, v11
	v_mul_f32_e32 v20, 0x3fb8aa3b, v20
	v_mul_f32_e32 v12, 0x3fb8aa3b, v12
	v_mul_f32_e32 v21, 0x3fb8aa3b, v21
	v_mul_f32_e32 v13, 0x3fb8aa3b, v13
	v_exp_f32_e32 v18, v18
	v_exp_f32_e32 v10, v10
	v_exp_f32_e32 v19, v19
	v_exp_f32_e32 v11, v11
	v_exp_f32_e32 v20, v20
	v_exp_f32_e32 v12, v12
	v_exp_f32_e32 v21, v21
	v_exp_f32_e32 v13, v13
	v_lshlrev_b32_e32 v6, 16, v22
	v_and_b32_e32 v7, 0xffff0000, v22
	v_fmac_f32_e32 v6, v4, v18
	v_fmac_f32_e32 v7, v5, v10
	v_lshlrev_b32_e32 v4, 16, v23
	v_and_b32_e32 v5, 0xffff0000, v23
	v_fmac_f32_e32 v4, v6, v19
	v_fmac_f32_e32 v5, v7, v11
	v_lshlrev_b32_e32 v6, 16, v24
	v_and_b32_e32 v7, 0xffff0000, v24
	v_fmac_f32_e32 v6, v4, v20
	v_fmac_f32_e32 v7, v5, v12
	v_lshlrev_b32_e32 v4, 16, v25
	v_and_b32_e32 v5, 0xffff0000, v25
	v_fmac_f32_e32 v4, v6, v21
	v_fmac_f32_e32 v5, v7, v13
	s_waitcnt vmcnt(12)
	v_permlane16_swap_b32_e32 v26, v27
	v_permlane16_swap_b32_e32 v28, v29
	v_permlane16_swap_b32_e32 v30, v31
	v_permlane16_swap_b32_e32 v32, v33
	v_permlane32_swap_b32_e32 v26, v28
	v_permlane32_swap_b32_e32 v27, v29
	v_permlane32_swap_b32_e32 v30, v32
	v_permlane32_swap_b32_e32 v31, v33
	v_and_b32_e32 v10, 0xffff0000, v26
	v_lshlrev_b32_e32 v26, 16, v26
	v_and_b32_e32 v11, 0xffff0000, v27
	v_lshlrev_b32_e32 v27, 16, v27
	v_and_b32_e32 v12, 0xffff0000, v28
	v_lshlrev_b32_e32 v28, 16, v28
	v_and_b32_e32 v13, 0xffff0000, v29
	v_lshlrev_b32_e32 v29, 16, v29
	v_add_f32_e32 v2, v2, v26
	v_add_f32_e32 v3, v3, v10
	v_add_f32_e32 v2, v2, v27
	v_add_f32_e32 v3, v3, v11
	v_add_f32_e32 v2, v2, v28
	v_add_f32_e32 v3, v3, v12
	v_add_f32_e32 v2, v2, v29
	v_add_f32_e32 v3, v3, v13
	v_mul_f32_e32 v26, 0x3fb8aa3b, v26
	v_mul_f32_e32 v10, 0x3fb8aa3b, v10
	v_mul_f32_e32 v27, 0x3fb8aa3b, v27
	v_mul_f32_e32 v11, 0x3fb8aa3b, v11
	v_mul_f32_e32 v28, 0x3fb8aa3b, v28
	v_mul_f32_e32 v12, 0x3fb8aa3b, v12
	v_mul_f32_e32 v29, 0x3fb8aa3b, v29
	v_mul_f32_e32 v13, 0x3fb8aa3b, v13
	v_exp_f32_e32 v26, v26
	v_exp_f32_e32 v10, v10
	v_exp_f32_e32 v27, v27
	v_exp_f32_e32 v11, v11
	v_exp_f32_e32 v28, v28
	v_exp_f32_e32 v12, v12
	v_exp_f32_e32 v29, v29
	v_exp_f32_e32 v13, v13
	v_lshlrev_b32_e32 v6, 16, v30
	v_and_b32_e32 v7, 0xffff0000, v30
	v_fmac_f32_e32 v6, v4, v26
	v_fmac_f32_e32 v7, v5, v10
	v_lshlrev_b32_e32 v4, 16, v31
	v_and_b32_e32 v5, 0xffff0000, v31
	v_fmac_f32_e32 v4, v6, v27
	v_fmac_f32_e32 v5, v7, v11
	v_lshlrev_b32_e32 v6, 16, v32
	v_and_b32_e32 v7, 0xffff0000, v32
	v_fmac_f32_e32 v6, v4, v28
	v_fmac_f32_e32 v7, v5, v12
	v_lshlrev_b32_e32 v4, 16, v33
	v_and_b32_e32 v5, 0xffff0000, v33
	v_fmac_f32_e32 v4, v6, v29
	v_fmac_f32_e32 v5, v7, v13
	s_waitcnt vmcnt(10)
	v_permlane16_swap_b32_e32 v34, v35
	v_permlane16_swap_b32_e32 v36, v37
	v_permlane16_swap_b32_e32 v38, v39
	v_permlane16_swap_b32_e32 v40, v41
	v_permlane32_swap_b32_e32 v34, v36
	v_permlane32_swap_b32_e32 v35, v37
	v_permlane32_swap_b32_e32 v38, v40
	v_permlane32_swap_b32_e32 v39, v41
	v_and_b32_e32 v10, 0xffff0000, v34
	v_lshlrev_b32_e32 v34, 16, v34
	v_and_b32_e32 v11, 0xffff0000, v35
	v_lshlrev_b32_e32 v35, 16, v35
	v_and_b32_e32 v12, 0xffff0000, v36
	v_lshlrev_b32_e32 v36, 16, v36
	v_and_b32_e32 v13, 0xffff0000, v37
	v_lshlrev_b32_e32 v37, 16, v37
	v_add_f32_e32 v2, v2, v34
	v_add_f32_e32 v3, v3, v10
	v_add_f32_e32 v2, v2, v35
	v_add_f32_e32 v3, v3, v11
	v_add_f32_e32 v2, v2, v36
	v_add_f32_e32 v3, v3, v12
	v_add_f32_e32 v2, v2, v37
	v_add_f32_e32 v3, v3, v13
	v_mul_f32_e32 v34, 0x3fb8aa3b, v34
	v_mul_f32_e32 v10, 0x3fb8aa3b, v10
	v_mul_f32_e32 v35, 0x3fb8aa3b, v35
	v_mul_f32_e32 v11, 0x3fb8aa3b, v11
	v_mul_f32_e32 v36, 0x3fb8aa3b, v36
	v_mul_f32_e32 v12, 0x3fb8aa3b, v12
	v_mul_f32_e32 v37, 0x3fb8aa3b, v37
	v_mul_f32_e32 v13, 0x3fb8aa3b, v13
	v_exp_f32_e32 v34, v34
	v_exp_f32_e32 v10, v10
	v_exp_f32_e32 v35, v35
	v_exp_f32_e32 v11, v11
	v_exp_f32_e32 v36, v36
	v_exp_f32_e32 v12, v12
	v_exp_f32_e32 v37, v37
	v_exp_f32_e32 v13, v13
	v_lshlrev_b32_e32 v6, 16, v38
	v_and_b32_e32 v7, 0xffff0000, v38
	v_fmac_f32_e32 v6, v4, v34
	v_fmac_f32_e32 v7, v5, v10
	v_lshlrev_b32_e32 v4, 16, v39
	v_and_b32_e32 v5, 0xffff0000, v39
	v_fmac_f32_e32 v4, v6, v35
	v_fmac_f32_e32 v5, v7, v11
	v_lshlrev_b32_e32 v6, 16, v40
	v_and_b32_e32 v7, 0xffff0000, v40
	v_fmac_f32_e32 v6, v4, v36
	v_fmac_f32_e32 v7, v5, v12
	v_lshlrev_b32_e32 v4, 16, v41
	v_and_b32_e32 v5, 0xffff0000, v41
	v_fmac_f32_e32 v4, v6, v37
	v_fmac_f32_e32 v5, v7, v13
	s_waitcnt vmcnt(8)
; __device__ __forceinline__ float bf_lo(unsigned w) { return __uint_as_float(w << 16); }
; __device__ __forceinline__ float bf_hi(unsigned w) { return __uint_as_float(w & 0xffff0000u); }
; __device__ __forceinline__ void scan_s1(CTXA) {
;     ...
;     for (int it = F.gw; it < 2 * NB * 64 * 8; it += F.NGW) {
;         const int cg = it & 7, chunk = (it >> 3) & 63, b = (it >> 9) & 3, d = it >> 11;
;         const int ch = cg * 128 + 2 * F.lane;
;         const size_t e0 = (size_t)d * T * D + ((size_t)b * S + chunk * 64) * D + ch;
;         const unsigned* la = (const unsigned*)(LA + e0); const unsigned* bb = (const unsigned*)(BB + e0);
;         float A0 = 0.f, A1 = 0.f, B0 = 0.f, B1 = 0.f;
; #pragma unroll
;         for (int g = 0; g < 4; ++g) { unsigned wl[16], wb[16];
; #pragma unroll
;             for (int q = 0; q < 16; ++q) { const int tt = g * 16 + q, t = d ? 63 - tt : tt; wl[q] = la[(size_t)t * (D / 2)]; wb[q] = bb[(size_t)t * (D / 2)]; }
; #pragma unroll
;             for (int q = 0; q < 16; ++q) { const float l0 = bf_lo(wl[q]), l1 = bf_hi(wl[q]);
;                 A0 += l0; A1 += l1; B0 = __expf(l0) * B0 + bf_lo(wb[q]); B1 = __expf(l1) * B1 + bf_hi(wb[q]); } }
	v_permlane16_swap_b32_e32 v42, v43
	v_permlane16_swap_b32_e32 v44, v45
	v_permlane16_swap_b32_e32 v46, v47
	v_permlane16_swap_b32_e32 v48, v49
	v_permlane32_swap_b32_e32 v42, v44
	v_permlane32_swap_b32_e32 v43, v45
	v_permlane32_swap_b32_e32 v46, v48
	v_permlane32_swap_b32_e32 v47, v49
	v_and_b32_e32 v10, 0xffff0000, v42
	v_lshlrev_b32_e32 v42, 16, v42
	v_and_b32_e32 v11, 0xffff0000, v43
	v_lshlrev_b32_e32 v43, 16, v43
	v_and_b32_e32 v12, 0xffff0000, v44
	v_lshlrev_b32_e32 v44, 16, v44
	v_and_b32_e32 v13, 0xffff0000, v45
	v_lshlrev_b32_e32 v45, 16, v45
	v_add_f32_e32 v2, v2, v42
	v_add_f32_e32 v3, v3, v10
	v_add_f32_e32 v2, v2, v43
	v_add_f32_e32 v3, v3, v11
	v_add_f32_e32 v2, v2, v44
	v_add_f32_e32 v3, v3, v12
	v_add_f32_e32 v2, v2, v45
	v_add_f32_e32 v3, v3, v13
	v_mul_f32_e32 v42, 0x3fb8aa3b, v42
	v_mul_f32_e32 v10, 0x3fb8aa3b, v10
	v_mul_f32_e32 v43, 0x3fb8aa3b, v43
	v_mul_f32_e32 v11, 0x3fb8aa3b, v11
	v_mul_f32_e32 v44, 0x3fb8aa3b, v44
	v_mul_f32_e32 v12, 0x3fb8aa3b, v12
	v_mul_f32_e32 v45, 0x3fb8aa3b, v45
	v_mul_f32_e32 v13, 0x3fb8aa3b, v13
	v_exp_f32_e32 v42, v42
	v_exp_f32_e32 v10, v10
	v_exp_f32_e32 v43, v43
	v_exp_f32_e32 v11, v11
	v_exp_f32_e32 v44, v44
	v_exp_f32_e32 v12, v12
	v_exp_f32_e32 v45, v45
	v_exp_f32_e32 v13, v13
	v_lshlrev_b32_e32 v6, 16, v46
	v_and_b32_e32 v7, 0xffff0000, v46
	v_fmac_f32_e32 v6, v4, v42
	v_fmac_f32_e32 v7, v5, v10
	v_lshlrev_b32_e32 v4, 16, v47
	v_and_b32_e32 v5, 0xffff0000, v47
	v_fmac_f32_e32 v4, v6, v43
	v_fmac_f32_e32 v5, v7, v11
	v_lshlrev_b32_e32 v6, 16, v48
	v_and_b32_e32 v7, 0xffff0000, v48
	v_fmac_f32_e32 v6, v4, v44
	v_fmac_f32_e32 v7, v5, v12
	v_lshlrev_b32_e32 v4, 16, v49
	v_and_b32_e32 v5, 0xffff0000, v49
	v_fmac_f32_e32 v4, v6, v45
	v_fmac_f32_e32 v5, v7, v13
	s_waitcnt vmcnt(6)
	v_permlane16_swap_b32_e32 v50, v51
	v_permlane16_swap_b32_e32 v52, v53
	v_permlane16_swap_b32_e32 v54, v55
	v_permlane16_swap_b32_e32 v56, v57
	v_permlane32_swap_b32_e32 v50, v52
	v_permlane32_swap_b32_e32 v51, v53
	v_permlane32_swap_b32_e32 v54, v56
	v_permlane32_swap_b32_e32 v55, v57
	v_and_b32_e32 v10, 0xffff0000, v50
	v_lshlrev_b32_e32 v50, 16, v50
	v_and_b32_e32 v11, 0xffff0000, v51
	v_lshlrev_b32_e32 v51, 16, v51
	v_and_b32_e32 v12, 0xffff0000, v52
	v_lshlrev_b32_e32 v52, 16, v52
	v_and_b32_e32 v13, 0xffff0000, v53
	v_lshlrev_b32_e32 v53, 16, v53
	v_add_f32_e32 v2, v2, v50
	v_add_f32_e32 v3, v3, v10
	v_add_f32_e32 v2, v2, v51
	v_add_f32_e32 v3, v3, v11
	v_add_f32_e32 v2, v2, v52
	v_add_f32_e32 v3, v3, v12
	v_add_f32_e32 v2, v2, v53
	v_add_f32_e32 v3, v3, v13
	v_mul_f32_e32 v50, 0x3fb8aa3b, v50
	v_mul_f32_e32 v10, 0x3fb8aa3b, v10
	v_mul_f32_e32 v51, 0x3fb8aa3b, v51
	v_mul_f32_e32 v11, 0x3fb8aa3b, v11
	v_mul_f32_e32 v52, 0x3fb8aa3b, v52
	v_mul_f32_e32 v12, 0x3fb8aa3b, v12
	v_mul_f32_e32 v53, 0x3fb8aa3b, v53
	v_mul_f32_e32 v13, 0x3fb8aa3b, v13
	v_exp_f32_e32 v50, v50
	v_exp_f32_e32 v10, v10
	v_exp_f32_e32 v51, v51
	v_exp_f32_e32 v11, v11
	v_exp_f32_e32 v52, v52
	v_exp_f32_e32 v12, v12
	v_exp_f32_e32 v53, v53
	v_exp_f32_e32 v13, v13
	v_lshlrev_b32_e32 v6, 16, v54
	v_and_b32_e32 v7, 0xffff0000, v54
	v_fmac_f32_e32 v6, v4, v50
	v_fmac_f32_e32 v7, v5, v10
	v_lshlrev_b32_e32 v4, 16, v55
	v_and_b32_e32 v5, 0xffff0000, v55
	v_fmac_f32_e32 v4, v6, v51
	v_fmac_f32_e32 v5, v7, v11
	v_lshlrev_b32_e32 v6, 16, v56
	v_and_b32_e32 v7, 0xffff0000, v56
	v_fmac_f32_e32 v6, v4, v52
	v_fmac_f32_e32 v7, v5, v12
	v_lshlrev_b32_e32 v4, 16, v57
	v_and_b32_e32 v5, 0xffff0000, v57
	v_fmac_f32_e32 v4, v6, v53
	v_fmac_f32_e32 v5, v7, v13
	s_waitcnt vmcnt(4)
	v_permlane16_swap_b32_e32 v58, v59
	v_permlane16_swap_b32_e32 v60, v61
	v_permlane16_swap_b32_e32 v62, v63
	v_permlane16_swap_b32_e32 v64, v65
	v_permlane32_swap_b32_e32 v58, v60
	v_permlane32_swap_b32_e32 v59, v61
	v_permlane32_swap_b32_e32 v62, v64
	v_permlane32_swap_b32_e32 v63, v65
	v_and_b32_e32 v10, 0xffff0000, v58
	v_lshlrev_b32_e32 v58, 16, v58
	v_and_b32_e32 v11, 0xffff0000, v59
	v_lshlrev_b32_e32 v59, 16, v59
	v_and_b32_e32 v12, 0xffff0000, v60
	v_lshlrev_b32_e32 v60, 16, v60
	v_and_b32_e32 v13, 0xffff0000, v61
	v_lshlrev_b32_e32 v61, 16, v61
	v_add_f32_e32 v2, v2, v58
	v_add_f32_e32 v3, v3, v10
	v_add_f32_e32 v2, v2, v59
	v_add_f32_e32 v3, v3, v11
	v_add_f32_e32 v2, v2, v60
	v_add_f32_e32 v3, v3, v12
	v_add_f32_e32 v2, v2, v61
	v_add_f32_e32 v3, v3, v13
	v_mul_f32_e32 v58, 0x3fb8aa3b, v58
	v_mul_f32_e32 v10, 0x3fb8aa3b, v10
	v_mul_f32_e32 v59, 0x3fb8aa3b, v59
	v_mul_f32_e32 v11, 0x3fb8aa3b, v11
	v_mul_f32_e32 v60, 0x3fb8aa3b, v60
	v_mul_f32_e32 v12, 0x3fb8aa3b, v12
	v_mul_f32_e32 v61, 0x3fb8aa3b, v61
	v_mul_f32_e32 v13, 0x3fb8aa3b, v13
	v_exp_f32_e32 v58, v58
	v_exp_f32_e32 v10, v10
	v_exp_f32_e32 v59, v59
	v_exp_f32_e32 v11, v11
	v_exp_f32_e32 v60, v60
	v_exp_f32_e32 v12, v12
	v_exp_f32_e32 v61, v61
	v_exp_f32_e32 v13, v13
	v_lshlrev_b32_e32 v6, 16, v62
	v_and_b32_e32 v7, 0xffff0000, v62
	v_fmac_f32_e32 v6, v4, v58
	v_fmac_f32_e32 v7, v5, v10
	v_lshlrev_b32_e32 v4, 16, v63
	v_and_b32_e32 v5, 0xffff0000, v63
	v_fmac_f32_e32 v4, v6, v59
	v_fmac_f32_e32 v5, v7, v11
	v_lshlrev_b32_e32 v6, 16, v64
	v_and_b32_e32 v7, 0xffff0000, v64
	v_fmac_f32_e32 v6, v4, v60
	v_fmac_f32_e32 v7, v5, v12
	v_lshlrev_b32_e32 v4, 16, v65
	v_and_b32_e32 v5, 0xffff0000, v65
	v_fmac_f32_e32 v4, v6, v61
	v_fmac_f32_e32 v5, v7, v13
	s_waitcnt vmcnt(2)
; __device__ __forceinline__ float bf_lo(unsigned w) { return __uint_as_float(w << 16); }
; __device__ __forceinline__ float bf_hi(unsigned w) { return __uint_as_float(w & 0xffff0000u); }
; __device__ __forceinline__ void scan_s1(CTXA) {
;     ...
;     for (int it = F.gw; it < 2 * NB * 64 * 8; it += F.NGW) {
;         const int cg = it & 7, chunk = (it >> 3) & 63, b = (it >> 9) & 3, d = it >> 11;
;         const int ch = cg * 128 + 2 * F.lane;
;         const size_t e0 = (size_t)d * T * D + ((size_t)b * S + chunk * 64) * D + ch;
;         const unsigned* la = (const unsigned*)(LA + e0); const unsigned* bb = (const unsigned*)(BB + e0);
;         float A0 = 0.f, A1 = 0.f, B0 = 0.f, B1 = 0.f;
; #pragma unroll
;         for (int g = 0; g < 4; ++g) { unsigned wl[16], wb[16];
; #pragma unroll
;             for (int q = 0; q < 16; ++q) { const int tt = g * 16 + q, t = d ? 63 - tt : tt; wl[q] = la[(size_t)t * (D / 2)]; wb[q] = bb[(size_t)t * (D / 2)]; }
; #pragma unroll
;             for (int q = 0; q < 16; ++q) { const float l0 = bf_lo(wl[q]), l1 = bf_hi(wl[q]);
;                 A0 += l0; A1 += l1; B0 = __expf(l0) * B0 + bf_lo(wb[q]); B1 = __expf(l1) * B1 + bf_hi(wb[q]); } }
;         const size_t o = ((size_t)((d * NB + b) * 64 + chunk)) * D + ch;
;         *(f32x2*)(CA + o) = (f32x2){A0, A1}; *(f32x2*)(CB + o) = (f32x2){B0, B1};
	v_permlane16_swap_b32_e32 v68, v69
	v_permlane16_swap_b32_e32 v70, v71
	v_permlane16_swap_b32_e32 v72, v73
	v_permlane16_swap_b32_e32 v74, v75
	v_permlane32_swap_b32_e32 v68, v70
	v_permlane32_swap_b32_e32 v69, v71
	v_permlane32_swap_b32_e32 v72, v74
	v_permlane32_swap_b32_e32 v73, v75
	v_and_b32_e32 v10, 0xffff0000, v68
	v_lshlrev_b32_e32 v68, 16, v68
	v_and_b32_e32 v11, 0xffff0000, v69
	v_lshlrev_b32_e32 v69, 16, v69
	v_and_b32_e32 v12, 0xffff0000, v70
	v_lshlrev_b32_e32 v70, 16, v70
	v_and_b32_e32 v13, 0xffff0000, v71
	v_lshlrev_b32_e32 v71, 16, v71
	v_add_f32_e32 v2, v2, v68
	v_add_f32_e32 v3, v3, v10
	v_add_f32_e32 v2, v2, v69
	v_add_f32_e32 v3, v3, v11
	v_add_f32_e32 v2, v2, v70
	v_add_f32_e32 v3, v3, v12
	v_add_f32_e32 v2, v2, v71
	v_add_f32_e32 v3, v3, v13
	v_mul_f32_e32 v68, 0x3fb8aa3b, v68
	v_mul_f32_e32 v10, 0x3fb8aa3b, v10
	v_mul_f32_e32 v69, 0x3fb8aa3b, v69
	v_mul_f32_e32 v11, 0x3fb8aa3b, v11
	v_mul_f32_e32 v70, 0x3fb8aa3b, v70
	v_mul_f32_e32 v12, 0x3fb8aa3b, v12
	v_mul_f32_e32 v71, 0x3fb8aa3b, v71
	v_mul_f32_e32 v13, 0x3fb8aa3b, v13
	v_exp_f32_e32 v68, v68
	v_exp_f32_e32 v10, v10
	v_exp_f32_e32 v69, v69
	v_exp_f32_e32 v11, v11
	v_exp_f32_e32 v70, v70
	v_exp_f32_e32 v12, v12
	v_exp_f32_e32 v71, v71
	v_exp_f32_e32 v13, v13
	v_lshlrev_b32_e32 v6, 16, v72
	v_and_b32_e32 v7, 0xffff0000, v72
	v_fmac_f32_e32 v6, v4, v68
	v_fmac_f32_e32 v7, v5, v10
	v_lshlrev_b32_e32 v4, 16, v73
	v_and_b32_e32 v5, 0xffff0000, v73
	v_fmac_f32_e32 v4, v6, v69
	v_fmac_f32_e32 v5, v7, v11
	v_lshlrev_b32_e32 v6, 16, v74
	v_and_b32_e32 v7, 0xffff0000, v74
	v_fmac_f32_e32 v6, v4, v70
	v_fmac_f32_e32 v7, v5, v12
	v_lshlrev_b32_e32 v4, 16, v75
	v_and_b32_e32 v5, 0xffff0000, v75
	v_fmac_f32_e32 v4, v6, v71
	v_fmac_f32_e32 v5, v7, v13
	s_waitcnt vmcnt(0)
	v_permlane16_swap_b32_e32 v76, v77
	v_permlane16_swap_b32_e32 v78, v79
	v_permlane16_swap_b32_e32 v80, v81
	v_permlane16_swap_b32_e32 v82, v83
	v_permlane32_swap_b32_e32 v76, v78
	v_permlane32_swap_b32_e32 v77, v79
	v_permlane32_swap_b32_e32 v80, v82
	v_permlane32_swap_b32_e32 v81, v83
	v_and_b32_e32 v10, 0xffff0000, v76
	v_lshlrev_b32_e32 v76, 16, v76
	v_and_b32_e32 v11, 0xffff0000, v77
	v_lshlrev_b32_e32 v77, 16, v77
	v_and_b32_e32 v12, 0xffff0000, v78
	v_lshlrev_b32_e32 v78, 16, v78
	v_and_b32_e32 v13, 0xffff0000, v79
	v_lshlrev_b32_e32 v79, 16, v79
	v_add_f32_e32 v2, v2, v76
	v_add_f32_e32 v3, v3, v10
	v_add_f32_e32 v2, v2, v77
	v_add_f32_e32 v3, v3, v11
	v_add_f32_e32 v2, v2, v78
	v_add_f32_e32 v3, v3, v12
	v_add_f32_e32 v2, v2, v79
	v_add_f32_e32 v3, v3, v13
	v_mul_f32_e32 v76, 0x3fb8aa3b, v76
	v_mul_f32_e32 v10, 0x3fb8aa3b, v10
	v_mul_f32_e32 v77, 0x3fb8aa3b, v77
	v_mul_f32_e32 v11, 0x3fb8aa3b, v11
	v_mul_f32_e32 v78, 0x3fb8aa3b, v78
	v_mul_f32_e32 v12, 0x3fb8aa3b, v12
	v_mul_f32_e32 v79, 0x3fb8aa3b, v79
	v_mul_f32_e32 v13, 0x3fb8aa3b, v13
	v_exp_f32_e32 v76, v76
	v_exp_f32_e32 v10, v10
	v_exp_f32_e32 v77, v77
	v_exp_f32_e32 v11, v11
	v_exp_f32_e32 v78, v78
	v_exp_f32_e32 v12, v12
	v_exp_f32_e32 v79, v79
	v_exp_f32_e32 v13, v13
	v_lshlrev_b32_e32 v6, 16, v80
	v_and_b32_e32 v7, 0xffff0000, v80
	v_fmac_f32_e32 v6, v4, v76
	v_fmac_f32_e32 v7, v5, v10
	v_lshlrev_b32_e32 v4, 16, v81
	v_and_b32_e32 v5, 0xffff0000, v81
	v_fmac_f32_e32 v4, v6, v77
	v_fmac_f32_e32 v5, v7, v11
	v_lshlrev_b32_e32 v6, 16, v82
	v_and_b32_e32 v7, 0xffff0000, v82
	v_fmac_f32_e32 v6, v4, v78
	v_fmac_f32_e32 v7, v5, v12
	v_lshlrev_b32_e32 v4, 16, v83
	v_and_b32_e32 v5, 0xffff0000, v83
	v_fmac_f32_e32 v4, v6, v79
	v_fmac_f32_e32 v5, v7, v13
	s_lshl_b32 s2, s16, 8
	s_lshl_b32 s9, s9, 6
	s_or_b32 s2, s9, s2
	s_or_b32 s8, s2, s8
	s_lshl_b32 s8, s8, 12
	v_lshl_or_b32 v9, v14, 2, s8
	s_add_i32 s0, s0, s1
	s_add_i32 s6, s6, s7
	global_store_dwordx2 v9, v[2:3], s[36:37]
	global_store_dwordx2 v9, v[4:5], s[40:41]
	s_cmpk_gt_i32 s0, 0xfff
	s_cbranch_scc0 .LBB0_194
